# baseline (speedup 1.0000x reference)
.LBB3_10:
	v_mov_b32_e32 v1, v0
	v_mov_b32_e32 v19, v103
	v_mov_b32_e32 v18, v102
	v_mov_b32_e32 v17, v101
	v_mov_b32_e32 v16, v100
	s_waitcnt lgkmcnt(0)
	s_nop 1
	v_permlane16_swap_b32_e32 v0, v1
	v_add_f32_e32 v0, v0, v1
	v_mov_b32_e32 v1, v0
	v_mov_b32_e32 v15, v107
	v_mov_b32_e32 v14, v106
	v_mov_b32_e32 v13, v105
	v_mov_b32_e32 v12, v104
	s_waitcnt lgkmcnt(0)
	s_nop 1
	v_permlane32_swap_b32_e32 v0, v1
	v_add_f32_e32 v0, v0, v1
	v_div_scale_f32 v1, s[4:5], v0, v0, 1.0
	v_rcp_f32_e32 v11, v1
	v_div_scale_f32 v21, vcc, 1.0, v0, 1.0
	v_mov_b32_e32 v6, v108
	v_fma_f32 v22, -v1, v11, 1.0
	v_fmac_f32_e32 v11, v22, v11
	v_mul_f32_e32 v22, v21, v11
	v_fma_f32 v23, -v1, v22, v21
	v_fmac_f32_e32 v22, v23, v11
	v_fma_f32 v1, -v1, v22, v21
	v_div_fmas_f32 v1, v1, v11, v22
	v_div_fixup_f32 v0, v1, v0, 1.0
	v_fma_mixlo_f16 v1, v0, v16, 0
	v_mov_b32_e32 v16, v17
	v_mov_b32_e32 v17, v18
	v_pk_mul_f32 v[16:17], v[0:1], v[16:17] op_sel_hi:[0,1]
	v_cvt_pk_f16_f32 v11, v16, v17
	v_pack_b32_f16 v16, v1, v11
	v_fma_mixlo_f16 v1, v0, v19, 0
	v_alignbit_b32 v17, v1, v11, 16
	v_fma_mixlo_f16 v1, v0, v12, 0
	v_mov_b32_e32 v12, v13
	v_mov_b32_e32 v13, v14
	v_pk_mul_f32 v[12:13], v[0:1], v[12:13] op_sel_hi:[0,1]
	v_cvt_pk_f16_f32 v11, v12, v13
	v_mov_b32_e32 v7, v109
	v_mov_b32_e32 v8, v110
	v_pack_b32_f16 v12, v1, v11
	v_fma_mixlo_f16 v1, v0, v15, 0
	s_lshl_b32 s3, s2, 6
	v_alignbit_b32 v13, v1, v11, 16
	v_fma_mixlo_f16 v1, v0, v6, 0
	v_mov_b32_e32 v6, v7
	v_mov_b32_e32 v7, v8
	s_and_b32 s3, s3, 0x400
	v_pk_mul_f32 v[6:7], v[0:1], v[6:7] op_sel_hi:[0,1]
	v_mov_b32_e32 v2, v112
	v_mov_b32_e32 v9, v111
	v_add_u32_e32 v20, s3, v32
	v_cvt_pk_f16_f32 v7, v6, v7
	v_mov_b32_e32 v3, v113
	v_mov_b32_e32 v4, v114
	v_or_b32_e32 v20, v20, v31
	v_mov_b32_e32 v21, 0
	v_pack_b32_f16 v6, v1, v7
	v_fma_mixlo_f16 v1, v0, v9, 0
	v_lshlrev_b64 v[22:23], 11, v[20:21]
	s_lshl_b32 s3, s2, 7
	v_alignbit_b32 v7, v1, v7, 16
	v_fma_mixlo_f16 v1, v0, v2, 0
	v_mov_b32_e32 v2, v3
	v_mov_b32_e32 v3, v4
	v_mov_b32_e32 v5, v115
	s_mov_b32 s5, 0
	v_lshl_add_u64 v[22:23], s[10:11], 0, v[22:23]
	s_and_b32 s4, s3, 0x780
	v_pk_mul_f32 v[2:3], v[0:1], v[2:3] op_sel_hi:[0,1]
	v_lshl_add_u64 v[22:23], v[22:23], 0, s[4:5]
	v_lshlrev_b32_e32 v20, 1, v33
	v_cvt_pk_f16_f32 v3, v2, v3
	v_fma_mixlo_f16 v0, v0, v5, 0
	v_lshl_add_u64 v[20:21], v[22:23], 0, v[20:21]
	v_pack_b32_f16 v2, v1, v3
	v_alignbit_b32 v3, v0, v3, 16
	s_mov_b64 s[4:5], 0
	global_store_dwordx2 v[20:21], v[16:17], off
	global_store_dwordx2 v[20:21], v[12:13], off offset:32
	global_store_dwordx2 v[20:21], v[6:7], off offset:64
	global_store_dwordx2 v[20:21], v[2:3], off offset:96

.LBB3_14:
	s_endpgm
	s_endpgm
	s_endpgm
	s_endpgm
	s_endpgm
	s_endpgm
	s_endpgm
	s_endpgm
	s_endpgm
	s_endpgm
	s_endpgm
	s_endpgm
	s_endpgm
	s_endpgm
	s_endpgm
	s_endpgm
	.section	.rodata,"a",@progbits
	.p2align	6, 0x0
